# 64 MoE-phase helpers (24576 layer-1 items) + 40 proj-phase helpers (18432 layer-0 MoE items); prologue converts the rest
# baseline (speedup 1.0000x reference)
;     ...
;             const int itB = it + NGW;
;             if (itB < NIT) { dB = decode(NIT - 1 - itB); tr_load(dB, vB); }
.Lps_1:
	s_cmp_lt_i32 s44, 0x7e80
	s_cbranch_scc1 .Lpt_1
	s_cmp_ge_i32 s44, 0xc680
	s_cbranch_scc1 .Lpt_1
	s_add_i32 s44, s44, 0x4800

;     ...
;             const int itA = itB + NGW;
;             if (itA < NIT) { dA = decode(NIT - 1 - itA); tr_load(dA, vA); }
.Lps_2:
	s_cmp_lt_i32 s42, 0x7e80
	s_cbranch_scc1 .Lpt_2
	s_cmp_ge_i32 s42, 0xc680
	s_cbranch_scc1 .Lpt_2
	s_add_i32 s42, s42, 0x4800

;     ...
;         auto decode = [&](int it) -> TrDesc {
;             TrDesc d; d.zero = 0; d.rope = 0; d.f8 = 0;
;             const int l = it / C_L; int r = it % C_L;
;             const float* W; unsigned char* WT; int ldw, K, k0, n0, scol, esz = 2;
;             if (r < C_IN) { const int kb = r / 188, nb = r % 188; n0 = 64 * nb; k0 = 64 * kb; ldw = NIN; K = D; W = a.w_in + (size_t)l * D * NIN;
;                 if (n0 < 3072) { d.rope = 1; scol = (n0 >> 7) * 128 + 32 * ((n0 >> 6) & 1) + 64 * (q4 >> 3) + 4 * (q4 & 7); }
;                 else if (n0 < 7680) scol = n0 + 4 * q4;
;                 else if (n0 < 11776) scol = n0 + 16 + 4 * q4;
;                 else if (n0 == 11776) { scol = (q4 < 4) ? 7680 + 4 * q4 : 0; d.zero = (q4 < 4) ? 0 : 1; }
;                 else { scol = 0; d.zero = 1; }
;     ...
;                 d.f8 = 1; esz = 1; WT = ws + WS_WIN + (size_t)l * NP * D;
;     ...
;                 WT = ws + WS_WIN + (size_t)l * NP * D * 2;
;     ...
;             } else if ((r -= C_IN) < C_OA) { const int kb = r / 32, nb = r % 32; n0 = 64 * nb; k0 = 64 * kb; ldw = D; K = 512; scol = n0 + 4 * q4; W = a.w_out_a + (size_t)l * 512 * D; WT = ws + WS_WOA + (size_t)l * D * 512 * (MIX_F8 ? 1 : 2); if (MIX_F8) { d.f8 = 1; esz = 1; }
;                 if (BR_FUSE) { K = 1536; WT = ws + WS_WOA + (size_t)l * D * 1536 + 1024; }
;             } else if ((r -= C_OA) < C_OB) { const int kb = r / 32, nb = r % 32; n0 = 64 * nb; k0 = 64 * kb; ldw = D; K = 1024; scol = n0 + 4 * q4; W = a.w_out_b + (size_t)l * 1024 * D; WT = ws + WS_WOB + (size_t)l * D * 1024 * (MIX_F8 ? 1 : 2); if (MIX_F8) { d.f8 = 1; esz = 1; }
;                 if (BR_FUSE) { K = 1536; WT = ws + WS_WOA + (size_t)l * D * 1536; }
; template <unsigned MASK, bool ONE>
; __global__ void __launch_bounds__(NTHREADS, 2) fwd_kernel(Args a_unused) {
;     ...
;         if (IN(P + 1, 2)) { FRESH_TID();
;     ...
;             pg8::StaticOrderP S{T / 256, NP / 256, G, bx}; pg8::RowsContig AM; pg8::EpiProj E{proj, ropec, ropes, alow, pg8::W8_INV};
;             pg8::gemm_phase<pg8::EpiProj, pg8::StaticOrderP, pg8::RowsContig, true, true>(lds, tid, hbuf, (const bf16_t*)(ws + WS_WIN + (size_t)l * NP * D), 0, D / 2, S, AM, E);
.LBB0_265:
	s_or_b64 exec, exec, s[0:1]
	v_readlane_b32 s0, v253, 0
	v_readlane_b32 s1, v253, 1
	s_mov_b32 s2, s38
	s_waitcnt lgkmcnt(0)
	s_barrier
	s_nop 0
	v_mbcnt_lo_u32_b32 v0, s2, 0
	v_mbcnt_hi_u32_b32 v0, s2, v0
	v_readlane_b32 s2, v253, 7
	v_readlane_b32 s3, v253, 8
	v_add_u32_e32 v1, s78, v0
	s_andn2_b64 vcc, exec, s[2:3]
	v_readfirstlane_b32 s16, v1
	v_readlane_b32 s101, v255, 17
	s_movk_i32 s100, 0x100
	s_cmp_eq_u32 s101, 0
	s_cbranch_scc0 .Lpq_skip
	s_movk_i32 s100, 0xd8
	v_readlane_b32 s101, v253, 4
	s_nop 1
	s_cmp_lt_i32 s101, s100
	s_cbranch_scc1 .Lpq_skip
	s_mov_b32 s100, 0x7e80
	s_mov_b32 s101, 0xc680
	v_writelane_b32 v251, s16, 0
	v_writelane_b32 v251, s17, 1
	v_writelane_b32 v251, s18, 2
	v_writelane_b32 v251, s19, 3
	v_writelane_b32 v251, s20, 4
	v_writelane_b32 v251, s21, 5
	v_writelane_b32 v251, s23, 6
	v_writelane_b32 v251, s25, 7
	v_writelane_b32 v251, s26, 8
	v_writelane_b32 v251, s33, 9
	v_writelane_b32 v251, s38, 10
	v_writelane_b32 v251, s39, 11
	v_writelane_b32 v251, s41, 12
	v_writelane_b32 v251, s42, 13
	v_writelane_b32 v251, s45, 14
	v_writelane_b32 v251, s48, 15
	v_writelane_b32 v251, s49, 16
	v_writelane_b32 v251, s50, 17
	v_writelane_b32 v251, s51, 18
	v_writelane_b32 v251, s74, 19
	v_writelane_b32 v251, s76, 20
	v_mov_b32_e32 v193, v3
	v_mov_b32_e32 v194, v33
	v_mov_b32_e32 v195, v59
	v_mov_b32_e32 v196, v63
	v_mov_b32_e32 v197, v110
	v_mov_b32_e32 v198, v111
	v_mov_b32_e32 v199, v114
	v_mov_b32_e32 v200, v115
	v_mov_b32_e32 v201, v149
	v_mov_b32_e32 v202, v153
	v_mov_b32_e32 v203, v157
	v_mov_b32_e32 v204, v161
	v_mov_b32_e32 v205, v165
	v_mov_b32_e32 v206, v169
	v_mov_b32_e32 v207, v173
	v_mov_b32_e32 v208, v177
	v_mov_b32_e32 v209, v178
	v_mov_b32_e32 v210, v179
	v_mov_b32_e32 v211, v180
	v_mov_b32_e32 v212, v181
	v_mov_b32_e32 v214, v182
	v_mov_b32_e32 v215, v183
	v_mov_b32_e32 v216, v184
	v_mov_b32_e32 v218, v185
	v_readlane_b32 s76, v253, 4
	v_readlane_b32 s8, v253, 0
	v_readlane_b32 s9, v253, 1
	s_nop 1
	s_sub_i32 s0, s76, 216
	s_lshr_b32 s1, s100, 3
	s_add_i32 s0, s0, s1
	s_lshr_b32 s33, s78, 6
	s_lshr_b32 s1, s0, 3
	s_lshl_b32 s1, s1, 6
	s_and_b32 s0, s0, 7
	s_lshl_b32 s0, s0, 2
	s_or_b32 s1, s1, s0
	s_and_b32 s0, s33, 3
	s_or_b32 s1, s1, s0
	s_lshr_b32 s0, s33, 2
	s_lshl_b32 s0, s0, 5
	s_or_b32 s1, s1, s0
	s_sub_i32 s100, s1, s33
	s_mov_b32 s76, 0
	s_movk_i32 s74, 40
	s_load_dwordx2 s[10:11], s[8:9], 0xa0
	v_mbcnt_lo_u32_b32 v69, -1, 0
	v_mbcnt_hi_u32_b32 v69, -1, v69
	s_mov_b64 exec, -1
	v_lshlrev_b32_e32 v76, 3, v69
	s_waitcnt lgkmcnt(0)
	s_lshl_b32 s47, s76, 3
	s_add_i32 s47, s47, s33
	s_add_i32 s47, s47, s100
	v_and_b32_e32 v2, 15, v69
	s_cmp_ge_i32 s47, s101
	v_ashrrev_i32_e32 v133, 4, v69
	s_cbranch_scc1 .LBB0_36_hq
	s_sub_i32 s1, 0xfcff, s47
	s_mul_hi_u32 s0, s1, 0x81848da9
	s_lshr_b32 s0, s0, 14
	s_mul_i32 s2, s0, 0x7e80
	s_sub_i32 s17, s1, s2
	s_cmpk_gt_u32 s17, 0x177f
	s_cbranch_scc0 .LBB0_37_hq
	s_cmpk_gt_u32 s17, 0x187f
	s_cbranch_scc0 .LBB0_39_hq
	s_cmpk_gt_u32 s17, 0x1a7f
	s_cbranch_scc0 .LBB0_40_hq
	s_cmpk_gt_u32 s17, 0x1e7f
	s_cbranch_scc0 .LBB0_41_hq
	s_lshl_b32 s1, s17, 6
	s_cmpk_gt_u32 s17, 0x5e7f
	s_cbranch_scc0 .LBB0_42_hq
	s_add_i32 s2, s17, 0xffffa180
	s_lshr_b32 s4, s2, 9
	s_lshl_b32 s2, s2, 1
	s_and_b32 s18, s2, 0x3c0
	s_load_dwordx2 s[2:3], s[8:9], 0x88
	s_lshl_b32 s5, s0, 4
	s_add_i32 s6, s4, s5
	s_mov_b32 s7, 0
	s_and_b32 s16, s1, 0x7c0
	s_lshl_b64 s[4:5], s[6:7], 23
	s_waitcnt lgkmcnt(0)
	s_add_u32 s4, s2, s4
	s_addc_u32 s5, s3, s5
	s_lshl_b64 s[2:3], s[6:7], 21
	s_add_u32 s2, s10, s2
	s_addc_u32 s3, s11, s3
	s_add_u32 s6, s2, 0x18600000
	v_lshl_or_b32 v0, v2, 2, s16
	s_addc_u32 s7, s3, 0
	s_mov_b64 s[2:3], 0
	s_branch .LBB0_43_hq
